# di7a
# speedup vs baseline: 1.0398x; 1.0187x over previous
.LBB1_2:
	s_bitcmp1_b32 s22, 0
	s_cselect_b32 s2, 0x8800, 0
	v_add_u32_e32 v163, s2, v188
	ds_read_b128 v[236:239], v164
	s_add_i32 s10, s10, 1
	s_and_b32 s2, s10, 1
	v_lshl_or_b32 v165, s2, 15, v186
	s_mul_i32 s3, s2, 0x8800
	v_add_u32_e32 v201, s3, v187
	ds_read_b128 v[166:169], v165
	ds_read_b128 v[190:193], v201
	ds_read_b128 v[206:209], v165 offset:2048
	ds_read_b128 v[210:213], v165 offset:4096
	ds_read_b128 v[170:173], v165 offset:6144
	ds_read_b128 v[174:177], v201 offset:2176
	ds_read_b128 v[194:197], v201 offset:4352
	ds_read_b128 v[202:205], v201 offset:6528
	s_add_i32 s21, s35, 0x8000
	s_and_b32 s2, s21, 0x8000
	v_add_u32_e32 v164, s2, v189
	s_add_i32 s2, s4, s2
	s_add_i32 s3, s21, s48
	s_and_b32 s3, s3, 0x78000
	s_add_i32 s3, s3, s5
	s_add_i32 s42, s20, s49
	s_and_b32 s42, s42, 0xf00
	s_add_i32 s42, s42, s11
	s_add_i32 s23, s3, 0x0
	buffer_load_dwordx4 v[240:243], v189, s[12:15], s23 offen
	s_add_i32 s23, s3, 0x2000
	buffer_load_dwordx4 v[244:247], v189, s[12:15], s23 offen
	s_add_i32 s23, s3, 0x4000
	buffer_load_dwordx4 v[248:251], v189, s[12:15], s23 offen
	s_add_i32 s23, s3, 0x6000
	buffer_load_dwordx4 v[252:255], v189, s[12:15], s23 offen
	s_waitcnt lgkmcnt(7)
	s_waitcnt lgkmcnt(6)
	v_mfma_f32_16x16x32_f16 v[106:109], v[166:169], v[190:193], v[106:109]
	ds_read_b128 v[214:217], v165 offset:8192
	s_waitcnt lgkmcnt(6)
	v_mfma_f32_16x16x32_f16 v[98:101], v[206:209], v[190:193], v[98:101]
	ds_read_b128 v[218:221], v165 offset:10240
	s_waitcnt lgkmcnt(6)
	v_mfma_f32_16x16x32_f16 v[86:89], v[210:213], v[190:193], v[86:89]
	ds_read_b128 v[222:225], v165 offset:12288
	s_waitcnt lgkmcnt(6)
	v_mfma_f32_16x16x32_f16 v[82:85], v[170:173], v[190:193], v[82:85]
	ds_read_b128 v[226:229], v165 offset:14336
	s_waitcnt lgkmcnt(6)
	v_mfma_f32_16x16x32_f16 v[46:49], v[166:169], v[174:177], v[46:49]
	v_mfma_f32_16x16x32_f16 v[42:45], v[206:209], v[174:177], v[42:45]
	v_mfma_f32_16x16x32_f16 v[26:29], v[210:213], v[174:177], v[26:29]
	v_mfma_f32_16x16x32_f16 v[2:5], v[170:173], v[174:177], v[2:5]
	v_cvt_pk_f16_f32 v234, v236, v237
	s_waitcnt lgkmcnt(5)
	v_mfma_f32_16x16x32_f16 v[118:121], v[166:169], v[194:197], v[118:121]
	v_cvt_pk_f16_f32 v235, v238, v239
	v_mfma_f32_16x16x32_f16 v[122:125], v[206:209], v[194:197], v[122:125]
	s_waitcnt vmcnt(10)
	v_cvt_pk_f16_f32 v230, v10, v11
	v_mfma_f32_16x16x32_f16 v[134:137], v[210:213], v[194:197], v[134:137]
	v_cvt_pk_f16_f32 v231, v12, v13
	v_mfma_f32_16x16x32_f16 v[138:141], v[170:173], v[194:197], v[138:141]
	v_cvt_pk_f16_f32 v232, v14, v15
	s_waitcnt lgkmcnt(4)
	v_mfma_f32_16x16x32_f16 v[142:145], v[166:169], v[202:205], v[142:145]
	v_cvt_pk_f16_f32 v233, v16, v17
	ds_read_b128 v[166:169], v165 offset:1024
	v_mfma_f32_16x16x32_f16 v[146:149], v[206:209], v[202:205], v[146:149]
	v_dot2c_f32_f16_e32 v185, v230, v234
	ds_read_b128 v[206:209], v201 offset:1088
	v_mfma_f32_16x16x32_f16 v[154:157], v[210:213], v[202:205], v[154:157]
	v_dot2c_f32_f16_e32 v184, v232, v234
	ds_read_b128 v[210:213], v165 offset:3072
	v_mfma_f32_16x16x32_f16 v[150:153], v[170:173], v[202:205], v[150:153]
	v_dot2c_f32_f16_e32 v185, v231, v235
	ds_read_b128 v[170:173], v165 offset:5120
	s_waitcnt lgkmcnt(7)
	v_mfma_f32_16x16x32_f16 v[34:37], v[214:217], v[190:193], v[34:37]
	v_dot2c_f32_f16_e32 v184, v233, v235
	s_waitcnt lgkmcnt(6)
	v_mfma_f32_16x16x32_f16 v[22:25], v[218:221], v[190:193], v[22:25]
	ds_write2_b64 v163, v[230:231], v[232:233] offset1:8
	s_waitcnt lgkmcnt(6)
	v_mfma_f32_16x16x32_f16 v[18:21], v[222:225], v[190:193], v[18:21]
	s_add_i32 s43, s42, 0x0
	buffer_load_dwordx4 v[10:13], v1, s[16:19], s43 offen nt sc1
	s_waitcnt lgkmcnt(5)
	v_mfma_f32_16x16x32_f16 v[6:9], v[226:229], v[190:193], v[6:9]
	s_add_i32 s43, s42, 0x4000
	buffer_load_dwordx4 v[14:17], v1, s[16:19], s43 offen nt sc1
	ds_read_b128 v[190:193], v165 offset:7168
	v_mfma_f32_16x16x32_f16 v[58:61], v[214:217], v[174:177], v[58:61]
	s_waitcnt vmcnt(10)
	v_cvt_pk_f16_f32 v230, v30, v31
	v_mfma_f32_16x16x32_f16 v[62:65], v[218:221], v[174:177], v[62:65]
	v_cvt_pk_f16_f32 v231, v32, v33
	v_mfma_f32_16x16x32_f16 v[66:69], v[222:225], v[174:177], v[66:69]
	v_cvt_pk_f16_f32 v232, v38, v39
	v_mfma_f32_16x16x32_f16 v[70:73], v[226:229], v[174:177], v[70:73]
	v_cvt_pk_f16_f32 v233, v40, v41
	ds_read_b128 v[174:177], v201 offset:3264
	v_mfma_f32_16x16x32_f16 v[94:97], v[214:217], v[194:197], v[94:97]
	v_dot2c_f32_f16_e32 v183, v230, v234
	v_mfma_f32_16x16x32_f16 v[102:105], v[218:221], v[194:197], v[102:105]
	v_dot2c_f32_f16_e32 v181, v232, v234
	v_mfma_f32_16x16x32_f16 v[110:113], v[222:225], v[194:197], v[110:113]
	v_dot2c_f32_f16_e32 v183, v231, v235
	v_mfma_f32_16x16x32_f16 v[90:93], v[226:229], v[194:197], v[90:93]
	v_dot2c_f32_f16_e32 v181, v233, v235
	ds_read_b128 v[194:197], v201 offset:5440
	v_mfma_f32_16x16x32_f16 v[114:117], v[214:217], v[202:205], v[114:117]
	ds_write2_b64 v163, v[230:231], v[232:233] offset0:16 offset1:24
	ds_read_b128 v[214:217], v201 offset:7616
	v_mfma_f32_16x16x32_f16 v[126:129], v[218:221], v[202:205], v[126:129]
	v_add_u32_e32 v163, 0x800, v163
	ds_read_b128 v[218:221], v165 offset:9216
	v_mfma_f32_16x16x32_f16 v[130:133], v[222:225], v[202:205], v[130:133]
	s_add_i32 s43, s42, 0x8000
	buffer_load_dwordx4 v[30:33], v1, s[16:19], s43 offen nt sc1
	ds_read_b128 v[222:225], v165 offset:11264
	v_mfma_f32_16x16x32_f16 v[158:161], v[226:229], v[202:205], v[158:161]
	s_add_i32 s43, s42, 0xc000
	buffer_load_dwordx4 v[38:41], v1, s[16:19], s43 offen nt sc1
	ds_read_b128 v[226:229], v165 offset:13312
	s_waitcnt lgkmcnt(12)
	s_waitcnt lgkmcnt(11)
	v_mfma_f32_16x16x32_f16 v[106:109], v[166:169], v[206:209], v[106:109]
	s_waitcnt vmcnt(10)
	v_cvt_pk_f16_f32 v230, v50, v51
	ds_read_b128 v[202:205], v165 offset:15360
	s_waitcnt lgkmcnt(11)
	v_mfma_f32_16x16x32_f16 v[98:101], v[210:213], v[206:209], v[98:101]
	v_cvt_pk_f16_f32 v231, v52, v53
	s_waitcnt lgkmcnt(10)
	v_mfma_f32_16x16x32_f16 v[86:89], v[170:173], v[206:209], v[86:89]
	v_cvt_pk_f16_f32 v232, v54, v55
	s_waitcnt lgkmcnt(8)
	v_mfma_f32_16x16x32_f16 v[82:85], v[190:193], v[206:209], v[82:85]
	v_cvt_pk_f16_f32 v233, v56, v57
	s_waitcnt lgkmcnt(7)
	v_mfma_f32_16x16x32_f16 v[46:49], v[166:169], v[174:177], v[46:49]
	v_dot2c_f32_f16_e32 v182, v230, v234
	v_mfma_f32_16x16x32_f16 v[42:45], v[210:213], v[174:177], v[42:45]
	v_dot2c_f32_f16_e32 v178, v232, v234
	v_mfma_f32_16x16x32_f16 v[26:29], v[170:173], v[174:177], v[26:29]
	v_dot2c_f32_f16_e32 v182, v231, v235
	v_mfma_f32_16x16x32_f16 v[2:5], v[190:193], v[174:177], v[2:5]
	v_dot2c_f32_f16_e32 v178, v233, v235
	s_waitcnt lgkmcnt(6)
	v_mfma_f32_16x16x32_f16 v[118:121], v[166:169], v[194:197], v[118:121]
	ds_write2_b64 v163, v[230:231], v[232:233] offset0:16 offset1:24
	v_mfma_f32_16x16x32_f16 v[122:125], v[210:213], v[194:197], v[122:125]
	s_add_i32 s43, s42, 0x10000
	buffer_load_dwordx4 v[50:53], v1, s[16:19], s43 offen nt sc1
	v_mfma_f32_16x16x32_f16 v[134:137], v[170:173], v[194:197], v[134:137]
	s_add_i32 s43, s42, 0x14000
	buffer_load_dwordx4 v[54:57], v1, s[16:19], s43 offen nt sc1
	v_mfma_f32_16x16x32_f16 v[138:141], v[190:193], v[194:197], v[138:141]
	s_waitcnt vmcnt(10)
	v_cvt_pk_f16_f32 v230, v74, v75
	s_waitcnt lgkmcnt(5)
	v_mfma_f32_16x16x32_f16 v[142:145], v[166:169], v[214:217], v[142:145]
	v_cvt_pk_f16_f32 v231, v76, v77
	v_mfma_f32_16x16x32_f16 v[146:149], v[210:213], v[214:217], v[146:149]
	v_cvt_pk_f16_f32 v232, v78, v79
	v_mfma_f32_16x16x32_f16 v[154:157], v[170:173], v[214:217], v[154:157]
	v_cvt_pk_f16_f32 v233, v80, v81
	v_mfma_f32_16x16x32_f16 v[150:153], v[190:193], v[214:217], v[150:153]
	v_dot2c_f32_f16_e32 v179, v230, v234
	s_waitcnt lgkmcnt(4)
	v_mfma_f32_16x16x32_f16 v[34:37], v[218:221], v[206:209], v[34:37]
	v_dot2c_f32_f16_e32 v180, v232, v234
	s_waitcnt lgkmcnt(3)
	v_mfma_f32_16x16x32_f16 v[22:25], v[222:225], v[206:209], v[22:25]
	v_dot2c_f32_f16_e32 v179, v231, v235
	s_waitcnt lgkmcnt(2)
	v_mfma_f32_16x16x32_f16 v[18:21], v[226:229], v[206:209], v[18:21]
	v_dot2c_f32_f16_e32 v180, v233, v235
	s_waitcnt lgkmcnt(1)
	v_mfma_f32_16x16x32_f16 v[6:9], v[202:205], v[206:209], v[6:9]
	ds_write2_b64 v163, v[230:231], v[232:233] offset0:32 offset1:40
	v_mfma_f32_16x16x32_f16 v[58:61], v[218:221], v[174:177], v[58:61]
	s_add_i32 s43, s42, 0x18000
	buffer_load_dwordx4 v[74:77], v1, s[16:19], s43 offen nt sc1
	v_mfma_f32_16x16x32_f16 v[62:65], v[222:225], v[174:177], v[62:65]
	s_add_i32 s43, s42, 0x1c000
	buffer_load_dwordx4 v[78:81], v1, s[16:19], s43 offen nt sc1
	v_mfma_f32_16x16x32_f16 v[66:69], v[226:229], v[174:177], v[66:69]
	v_mfma_f32_16x16x32_f16 v[70:73], v[202:205], v[174:177], v[70:73]
	s_waitcnt vmcnt(11)
	ds_write_b128 v164, v[240:243]
	v_mfma_f32_16x16x32_f16 v[94:97], v[218:221], v[194:197], v[94:97]
	v_mfma_f32_16x16x32_f16 v[102:105], v[222:225], v[194:197], v[102:105]
	s_waitcnt vmcnt(10)
	ds_write_b128 v164, v[244:247] offset:8192
	v_mfma_f32_16x16x32_f16 v[110:113], v[226:229], v[194:197], v[110:113]
	v_mfma_f32_16x16x32_f16 v[90:93], v[202:205], v[194:197], v[90:93]
	s_waitcnt vmcnt(9)
	ds_write_b128 v164, v[248:251] offset:16384
	v_mfma_f32_16x16x32_f16 v[114:117], v[218:221], v[214:217], v[114:117]
	v_mfma_f32_16x16x32_f16 v[126:129], v[222:225], v[214:217], v[126:129]
	s_waitcnt vmcnt(8)
	ds_write_b128 v164, v[252:255] offset:24576
	v_mfma_f32_16x16x32_f16 v[130:133], v[226:229], v[214:217], v[130:133]
	v_mfma_f32_16x16x32_f16 v[158:161], v[202:205], v[214:217], v[158:161]
	s_waitcnt lgkmcnt(0)
	s_barrier
	s_addk_i32 s20, 0x100
	s_cmpk_eq_i32 s20, 0xe00
	s_cbranch_scc1 .Lmy_exit
	s_mov_b32 s35, s21
	s_add_i32 s22, s10, 2
	s_add_i32 s54, s20, s46
	s_and_b32 s54, s54, 0xf00
	v_add_u32_e32 v164, s54, v162
	s_branch .LBB1_2

	.amdhsa_kernel _Z11main_kernelPKfPKhS0_S0_Pf
		.amdhsa_group_segment_fixed_size 142336
		.amdhsa_private_segment_fixed_size 0
		.amdhsa_kernarg_size 40
		.amdhsa_user_sgpr_count 2
		.amdhsa_user_sgpr_dispatch_ptr 0
		.amdhsa_user_sgpr_queue_ptr 0
		.amdhsa_user_sgpr_kernarg_segment_ptr 1
		.amdhsa_user_sgpr_dispatch_id 0
		.amdhsa_user_sgpr_kernarg_preload_length 0
		.amdhsa_user_sgpr_kernarg_preload_offset 0
		.amdhsa_user_sgpr_private_segment_size 0
		.amdhsa_uses_dynamic_stack 0
		.amdhsa_enable_private_segment 0
		.amdhsa_system_sgpr_workgroup_id_x 1
		.amdhsa_system_sgpr_workgroup_id_y 0
		.amdhsa_system_sgpr_workgroup_id_z 0
		.amdhsa_system_sgpr_workgroup_info 0
		.amdhsa_system_vgpr_workitem_id 0
		.amdhsa_next_free_vgpr 256
		.amdhsa_next_free_sgpr 96
		.amdhsa_accum_offset 256
		.amdhsa_reserve_vcc 1
		.amdhsa_float_round_mode_32 0
		.amdhsa_float_round_mode_16_64 0
		.amdhsa_float_denorm_mode_32 3
		.amdhsa_float_denorm_mode_16_64 3
		.amdhsa_dx10_clamp 1
		.amdhsa_ieee_mode 1
		.amdhsa_fp16_overflow 0
		.amdhsa_tg_split 0
		.amdhsa_exception_fp_ieee_invalid_op 0
		.amdhsa_exception_fp_denorm_src 0
		.amdhsa_exception_fp_ieee_div_zero 0
		.amdhsa_exception_fp_ieee_overflow 0
		.amdhsa_exception_fp_ieee_underflow 0
		.amdhsa_exception_fp_ieee_inexact 0
		.amdhsa_exception_int_div_zero 0
	.end_amdhsa_kernel

amdhsa.kernels:
  - .agpr_count:     0
    .args:
      - .actual_access:  read_only
        .address_space:  global
        .offset:         0
        .size:           8
        .value_kind:     global_buffer
      - .actual_access:  read_only
        .address_space:  global
        .offset:         8
        .size:           8
        .value_kind:     global_buffer
      - .actual_access:  read_only
        .address_space:  global
        .offset:         16
        .size:           8
        .value_kind:     global_buffer
      - .actual_access:  write_only
        .address_space:  global
        .offset:         24
        .size:           8
        .value_kind:     global_buffer
    .group_segment_fixed_size: 0
    .kernarg_segment_align: 8
    .kernarg_segment_size: 32
    .language:       OpenCL C
    .language_version:
      - 2
      - 0
    .max_flat_workgroup_size: 256
    .name:           _Z11prep_kernelPKfS0_S0_Ph
    .private_segment_fixed_size: 0
    .sgpr_count:     16
    .sgpr_spill_count: 0
    .symbol:         _Z11prep_kernelPKfS0_S0_Ph.kd
    .uniform_work_group_size: 1
    .uses_dynamic_stack: false
    .vgpr_count:     23
    .vgpr_spill_count: 0
    .wavefront_size: 64
  - .agpr_count:     0
    .args:
      - .actual_access:  read_only
        .address_space:  global
        .offset:         0
        .size:           8
        .value_kind:     global_buffer
      - .actual_access:  read_only
        .address_space:  global
        .offset:         8
        .size:           8
        .value_kind:     global_buffer
      - .actual_access:  read_only
        .address_space:  global
        .offset:         16
        .size:           8
        .value_kind:     global_buffer
      - .actual_access:  read_only
        .address_space:  global
        .offset:         24
        .size:           8
        .value_kind:     global_buffer
      - .actual_access:  write_only
        .address_space:  global
        .offset:         32
        .size:           8
        .value_kind:     global_buffer
    .group_segment_fixed_size: 142336
    .kernarg_segment_align: 8
    .kernarg_segment_size: 40
    .language:       OpenCL C
    .language_version:
      - 2
      - 0
    .max_flat_workgroup_size: 512
    .name:           _Z11main_kernelPKfPKhS0_S0_Pf
    .private_segment_fixed_size: 0
    .sgpr_count:     47
    .sgpr_spill_count: 0
    .symbol:         _Z11main_kernelPKfPKhS0_S0_Pf.kd
    .uniform_work_group_size: 1
    .uses_dynamic_stack: false
    .vgpr_count:     256
    .vgpr_spill_count: 0
    .wavefront_size: 64
